# P3 loop3: next-trip loads prefetched into spare VGPRs ahead of stores (software pipeline), on top of combo2
# baseline (speedup 1.0000x reference)
; #define GAS __attribute__((address_space(1)))
; #define LAS __attribute__((address_space(3)))
; __device__ __forceinline__ void unpack8(const u32x4 v, float (&f)[8]) { f[0] = bflo(v.x); f[1] = bfhi(v.x); f[2] = bflo(v.y); f[3] = bfhi(v.y); f[4] = bflo(v.z); f[5] = bfhi(v.z); f[6] = bflo(v.w); f[7] = bfhi(v.w); }
; __device__ __forceinline__ u32x4 pack8(const float (&f)[8]) { u32x4 o; o.x = cvtpk(f[0], f[1]); o.y = cvtpk(f[2], f[3]); o.z = cvtpk(f[4], f[5]); o.w = cvtpk(f[6], f[7]); return o; }
; __device__ __forceinline__ void p3_rows2(int row0, const bf16* PROJ, const float* sc_w, const float* sc_nw, const float* ssd_nw, const float* SSQ, bf16* Y, LAS unsigned char* scr, int lane) {
;     ...
; #pragma unroll 2
;     for (int i = 0; i < 8; ++i) { const int c0 = (i * 64 + lane) * 8;
;         float f0[8], f1[8]; unpack8(*(const LAS u32x4*)(scr + c0 * 2), f0); unpack8(*(const LAS u32x4*)(scr + 8192 + c0 * 2), f1);
;         const f32x4 ga = *(const GAS f32x4*)(sc_nw + c0), gb = *(const GAS f32x4*)(sc_nw + c0 + 4); const float g[8] = {ga.x, ga.y, ga.z, ga.w, gb.x, gb.y, gb.z, gb.w};
; #pragma unroll
;         for (int j = 0; j < 8; ++j) { f0[j] *= rs0 * g[j]; f1[j] *= rs1 * g[j]; }
;         *(GAS u32x4*)(yrow + D_SSD + i * 512) = pack8(f0); *(GAS u32x4*)(yrow + D_MIX + D_SSD + i * 512) = pack8(f1); }
;     float gs0 = SSQ[(size_t)row0 * NH + lane], gs1 = SSQ[(size_t)(row0 + 1) * NH + lane];
;     gs0 += __shfl_xor(gs0, 1); gs0 += __shfl_xor(gs0, 2); gs0 += __shfl_xor(gs0, 4); gs1 += __shfl_xor(gs1, 1); gs1 += __shfl_xor(gs1, 2); gs1 += __shfl_xor(gs1, 4);
; #pragma unroll 2
.LBB0_487:
	global_load_dwordx4 v[32:35], v[2:3], off offset:-2064
	global_load_dwordx4 v[36:39], v[2:3], off offset:-2048
	ds_read_b128 v[40:43], v26
	ds_read_b128 v[44:47], v26 offset:8192
	v_lshl_add_u64 v[48:49], v[24:25], 0, s[0:1]
	v_add_co_u32_e32 v50, vcc, s37, v48
	s_waitcnt lgkmcnt(1)
	v_lshlrev_b32_e32 v27, 16, v40
	v_addc_co_u32_e32 v51, vcc, 0, v49, vcc
	v_and_b32_e32 v31, 0xffff0000, v40
	v_lshlrev_b32_e32 v40, 16, v41
	v_and_b32_e32 v41, 0xffff0000, v41
	v_lshlrev_b32_e32 v52, 16, v42
	s_waitcnt lgkmcnt(0)
	v_lshlrev_b32_e32 v54, 16, v44
	v_and_b32_e32 v44, 0xffff0000, v44
	v_lshlrev_b32_e32 v55, 16, v45
	v_and_b32_e32 v45, 0xffff0000, v45
	v_add_co_u32_e32 v48, vcc, s38, v48
	v_and_b32_e32 v42, 0xffff0000, v42
	v_lshlrev_b32_e32 v53, 16, v43
	v_and_b32_e32 v43, 0xffff0000, v43
	v_addc_co_u32_e32 v49, vcc, 0, v49, vcc
	v_lshlrev_b32_e32 v56, 16, v46
	v_and_b32_e32 v46, 0xffff0000, v46
	v_lshlrev_b32_e32 v57, 16, v47
	v_and_b32_e32 v47, 0xffff0000, v47
	s_add_u32 s0, s0, 0x800
	s_addc_u32 s1, s1, 0
	s_cmpk_eq_i32 s0, 0x2000
	s_waitcnt vmcnt(1)
	v_mul_f32_e32 v59, v8, v33
	v_mul_f32_e32 v33, v9, v33
	v_mul_f32_e32 v60, v8, v34
	v_mul_f32_e32 v34, v9, v34
	v_mul_f32_e32 v61, v8, v35
	v_mul_f32_e32 v35, v9, v35
	s_waitcnt vmcnt(0)
	v_mul_f32_e32 v62, v8, v36
	v_mul_f32_e32 v58, v8, v32
	v_mul_f32_e32 v32, v9, v32
	v_mul_f32_e32 v63, v8, v37
	v_mul_f32_e32 v64, v8, v38
	v_mul_f32_e32 v65, v8, v39
	v_mul_f32_e32 v44, v33, v44
	v_mul_f32_e32 v33, v60, v40
	v_mul_f32_e32 v40, v34, v55
	v_mul_f32_e32 v34, v61, v41
	v_mul_f32_e32 v41, v35, v45
	v_mul_f32_e32 v35, v62, v52
	v_mul_f32_e32 v36, v9, v36
	v_mul_f32_e32 v37, v9, v37
	v_mul_f32_e32 v38, v9, v38
	v_mul_f32_e32 v39, v9, v39
	v_mul_f32_e32 v27, v58, v27
	v_mul_f32_e32 v54, v32, v54
	v_mul_f32_e32 v31, v59, v31
	v_mul_f32_e32 v42, v63, v42
	v_mul_f32_e32 v45, v64, v53
	v_mul_f32_e32 v43, v65, v43
	v_cvt_pk_bf16_f32 v32, v27, v31
	v_cvt_pk_bf16_f32 v33, v33, v34
	v_cvt_pk_bf16_f32 v34, v35, v42
	v_cvt_pk_bf16_f32 v35, v45, v43
	v_mul_f32_e32 v36, v36, v56
	v_mul_f32_e32 v37, v37, v46
	v_mul_f32_e32 v38, v38, v57
	v_mul_f32_e32 v39, v39, v47
	global_store_dwordx4 v[50:51], v[32:35], off
	s_nop 1
	v_cvt_pk_bf16_f32 v32, v54, v44
	v_cvt_pk_bf16_f32 v33, v40, v41
	v_cvt_pk_bf16_f32 v34, v36, v37
	v_cvt_pk_bf16_f32 v35, v38, v39
	global_store_dwordx4 v[48:49], v[32:35], off
	global_load_dwordx4 v[32:35], v[2:3], off offset:-16
	s_nop 0
	global_load_dwordx4 v[36:39], v[2:3], off
	ds_read_b128 v[40:43], v26 offset:1024
	ds_read_b128 v[44:47], v26 offset:9216
	v_add_u32_e32 v26, 0x800, v26
	v_lshl_add_u64 v[2:3], v[2:3], 0, s[26:27]
	s_waitcnt lgkmcnt(1)
	v_lshlrev_b32_e32 v27, 16, v40
	v_and_b32_e32 v31, 0xffff0000, v40
	v_lshlrev_b32_e32 v40, 16, v41
	v_and_b32_e32 v41, 0xffff0000, v41
	v_lshlrev_b32_e32 v52, 16, v42
	s_waitcnt lgkmcnt(0)
	v_lshlrev_b32_e32 v54, 16, v44
	v_and_b32_e32 v44, 0xffff0000, v44
	v_lshlrev_b32_e32 v55, 16, v45
	v_and_b32_e32 v45, 0xffff0000, v45
	v_and_b32_e32 v42, 0xffff0000, v42
	v_lshlrev_b32_e32 v53, 16, v43
	v_and_b32_e32 v43, 0xffff0000, v43
	v_lshlrev_b32_e32 v56, 16, v46
	v_and_b32_e32 v46, 0xffff0000, v46
	v_lshlrev_b32_e32 v57, 16, v47
	v_and_b32_e32 v47, 0xffff0000, v47
	s_waitcnt vmcnt(1)
	v_mul_f32_e32 v59, v8, v33
	v_mul_f32_e32 v33, v9, v33
	v_mul_f32_e32 v60, v8, v34
	v_mul_f32_e32 v34, v9, v34
	v_mul_f32_e32 v61, v8, v35
	v_mul_f32_e32 v35, v9, v35
	s_waitcnt vmcnt(0)
	v_mul_f32_e32 v62, v8, v36
	v_mul_f32_e32 v58, v8, v32
	v_mul_f32_e32 v32, v9, v32
	v_mul_f32_e32 v63, v8, v37
	v_mul_f32_e32 v64, v8, v38
	v_mul_f32_e32 v65, v8, v39
	v_mul_f32_e32 v44, v33, v44
	v_mul_f32_e32 v33, v60, v40
	v_mul_f32_e32 v40, v34, v55
	v_mul_f32_e32 v34, v61, v41
	v_mul_f32_e32 v41, v35, v45
	v_mul_f32_e32 v35, v62, v52
	v_mul_f32_e32 v36, v9, v36
	v_mul_f32_e32 v37, v9, v37
	v_mul_f32_e32 v38, v9, v38
	v_mul_f32_e32 v39, v9, v39
	v_mul_f32_e32 v27, v58, v27
	v_mul_f32_e32 v54, v32, v54
	v_mul_f32_e32 v31, v59, v31
	v_mul_f32_e32 v42, v63, v42
	v_mul_f32_e32 v45, v64, v53
	v_mul_f32_e32 v43, v65, v43
	v_cvt_pk_bf16_f32 v32, v27, v31
	v_cvt_pk_bf16_f32 v33, v33, v34
	v_cvt_pk_bf16_f32 v34, v35, v42
	v_cvt_pk_bf16_f32 v35, v45, v43
	v_mul_f32_e32 v36, v36, v56
	v_mul_f32_e32 v37, v37, v46
	v_mul_f32_e32 v38, v38, v57
	v_mul_f32_e32 v39, v39, v47
	global_store_dwordx4 v[50:51], v[32:35], off offset:1024
	s_nop 1
	v_cvt_pk_bf16_f32 v32, v54, v44
	v_cvt_pk_bf16_f32 v33, v40, v41
	v_cvt_pk_bf16_f32 v34, v36, v37
	v_cvt_pk_bf16_f32 v35, v38, v39
	global_store_dwordx4 v[48:49], v[32:35], off offset:1024
	s_cbranch_scc0 .LBB0_487
	s_mov_b32 s44, s39
	s_mov_b32 s45, 0
	s_mov_b32 s48, s40
	s_mov_b32 s49, 0
	v_lshl_add_u64 v[216:217], v[24:25], 0, s[44:45]
	v_lshl_add_u64 v[218:219], v[24:25], 0, s[48:49]
	global_load_dwordx4 v[184:187], v[22:23], off offset:-2048
	global_load_dwordx4 v[188:191], v[22:23], off offset:-2064
	global_load_dwordx4 v[192:195], v[216:217], off
	global_load_dwordx4 v[196:199], v[218:219], off
	global_load_dwordx4 v[200:203], v[216:217], off offset:1024
	global_load_dwordx4 v[204:207], v[22:23], off
	global_load_dwordx4 v[208:211], v[22:23], off offset:-16
	global_load_dwordx4 v[212:215], v[218:219], off offset:1024
	s_lshl_b32 s0, s41, 1
	s_ashr_i32 s1, s0, 31
	s_lshl_b64 s[4:5], s[0:1], 8
	s_or_b32 s0, s0, 1
	s_ashr_i32 s1, s0, 31
	v_lshl_add_u64 v[2:3], v[12:13], 0, s[4:5]
	s_lshl_b64 s[0:1], s[0:1], 8
	global_load_dword v8, v[2:3], off
	v_lshl_add_u64 v[2:3], v[12:13], 0, s[0:1]
	global_load_dword v2, v[2:3], off
	v_lshlrev_b32_e32 v31, 2, v4
	s_mov_b64 s[30:31], 0
	v_mov_b64_e32 v[26:27], v[22:23]
	s_waitcnt vmcnt(1)
	ds_bpermute_b32 v3, v5, v8
	s_waitcnt vmcnt(0)
	ds_bpermute_b32 v5, v5, v2
	s_waitcnt lgkmcnt(1)
	v_add_f32_e32 v3, v8, v3
	ds_bpermute_b32 v8, v6, v3
	s_waitcnt lgkmcnt(1)
	v_add_f32_e32 v2, v2, v5
	ds_bpermute_b32 v5, v6, v2
	s_waitcnt lgkmcnt(1)
	v_add_f32_e32 v3, v3, v8
	ds_bpermute_b32 v6, v7, v3
	s_waitcnt lgkmcnt(1)
	v_add_f32_e32 v2, v2, v5
	ds_bpermute_b32 v5, v7, v2
	s_waitcnt lgkmcnt(1)
	v_add_f32_e32 v32, v3, v6
	s_waitcnt lgkmcnt(0)
	v_add_f32_e32 v33, v2, v5
; #define GAS __attribute__((address_space(1)))
; __device__ __forceinline__ void unpack8(const u32x4 v, float (&f)[8]) { f[0] = bflo(v.x); f[1] = bfhi(v.x); f[2] = bflo(v.y); f[3] = bfhi(v.y); f[4] = bflo(v.z); f[5] = bfhi(v.z); f[6] = bflo(v.w); f[7] = bfhi(v.w); }
; __device__ __forceinline__ u32x4 pack8(const float (&f)[8]) { u32x4 o; o.x = cvtpk(f[0], f[1]); o.y = cvtpk(f[2], f[3]); o.z = cvtpk(f[4], f[5]); o.w = cvtpk(f[6], f[7]); return o; }
; __device__ __forceinline__ void p3_rows2(int row0, const bf16* PROJ, const float* sc_w, const float* sc_nw, const float* ssd_nw, const float* SSQ, bf16* Y, LAS unsigned char* scr, int lane) {
;     ...
; #pragma unroll 2
;     for (int i = 0; i < 8; ++i) { const int c0 = (i * 64 + lane) * 8;
;         const float rg0 = 1.0f / sqrtf(__shfl(gs0, i * 8) * (1.f / 512.f) + EPS), rg1 = 1.0f / sqrtf(__shfl(gs1, i * 8) * (1.f / 512.f) + EPS);
;         float f0[8], f1[8]; unpack8(*(const GAS u32x4*)(yrow + i * 512), f0); unpack8(*(const GAS u32x4*)(yrow + D_MIX + i * 512), f1);
;         const f32x4 ga = *(const GAS f32x4*)(ssd_nw + c0), gb = *(const GAS f32x4*)(ssd_nw + c0 + 4); const float g[8] = {ga.x, ga.y, ga.z, ga.w, gb.x, gb.y, gb.z, gb.w};
; #pragma unroll
;         for (int j = 0; j < 8; ++j) { f0[j] *= rg0 * g[j]; f1[j] *= rg1 * g[j]; }
;         *(GAS u32x4*)(yrow + i * 512) = pack8(f0); *(GAS u32x4*)(yrow + D_MIX + i * 512) = pack8(f1); }
.LBB0_489:
	v_lshl_add_u64 v[34:35], v[24:25], 0, s[30:31]
	v_add_co_u32_e32 v42, vcc, s39, v34
	s_waitcnt vmcnt(8)
	v_mov_b32_e32 v6, v188
	v_mov_b32_e32 v7, v189
	v_mov_b32_e32 v8, v190
	v_mov_b32_e32 v9, v191
	v_addc_co_u32_e32 v43, vcc, 0, v35, vcc
	v_add_co_u32_e32 v44, vcc, s40, v34
	ds_bpermute_b32 v46, v31, v32
	s_nop 0
	v_addc_co_u32_e32 v45, vcc, 0, v35, vcc
	v_mov_b32_e32 v34, v192
	v_mov_b32_e32 v35, v193
	v_mov_b32_e32 v36, v194
	v_mov_b32_e32 v37, v195
	v_mov_b32_e32 v38, v196
	v_mov_b32_e32 v39, v197
	v_mov_b32_e32 v40, v198
	v_mov_b32_e32 v41, v199
	v_mov_b32_e32 v2, v184
	v_mov_b32_e32 v3, v185
	v_mov_b32_e32 v4, v186
	v_mov_b32_e32 v5, v187
	s_add_u32 s42, s30, 0x800
	s_and_b32 s42, s42, 0x1800
	s_add_u32 s44, s42, s39
	s_addc_u32 s45, 0, 0
	s_add_u32 s48, s42, s40
	s_addc_u32 s49, 0, 0
	s_lshl_b32 s42, s42, 1
	s_mov_b32 s43, 0
	v_lshl_add_u64 v[216:217], v[24:25], 0, s[44:45]
	v_lshl_add_u64 v[218:219], v[24:25], 0, s[48:49]
	v_lshl_add_u64 v[220:221], v[22:23], 0, s[42:43]
	global_load_dwordx4 v[184:187], v[220:221], off offset:-2048
	global_load_dwordx4 v[188:191], v[220:221], off offset:-2064
	global_load_dwordx4 v[192:195], v[216:217], off
	global_load_dwordx4 v[196:199], v[218:219], off
	ds_bpermute_b32 v47, v31, v33
	ds_bpermute_b32 v48, v31, v32 offset:32
	ds_bpermute_b32 v49, v31, v33 offset:32
	s_waitcnt lgkmcnt(3)
	v_fmamk_f32 v46, v46, 0x3b000000, v28
	v_mul_f32_e32 v50, 0x4f800000, v46
	s_waitcnt lgkmcnt(2)
	v_fmamk_f32 v47, v47, 0x3b000000, v28
	s_waitcnt lgkmcnt(1)
	v_fmamk_f32 v48, v48, 0x3b000000, v28
	v_cmp_gt_f32_e64 s[6:7], s36, v46
	v_mul_f32_e32 v51, 0x4f800000, v47
	v_cmp_gt_f32_e32 vcc, s36, v47
	v_mul_f32_e32 v52, 0x4f800000, v48
	v_cmp_gt_f32_e64 s[0:1], s36, v48
	v_cndmask_b32_e64 v46, v46, v50, s[6:7]
	s_waitcnt lgkmcnt(0)
	v_fmamk_f32 v49, v49, 0x3b000000, v28
	v_cndmask_b32_e32 v47, v47, v51, vcc
	v_cndmask_b32_e64 v48, v48, v52, s[0:1]
	v_sqrt_f32_e32 v50, v46
	v_mul_f32_e32 v53, 0x4f800000, v49
	v_cmp_gt_f32_e64 s[4:5], s36, v49
	v_sqrt_f32_e32 v51, v47
	v_sqrt_f32_e32 v52, v48
	v_cndmask_b32_e64 v49, v49, v53, s[4:5]
	v_sqrt_f32_e32 v53, v49
	v_add_u32_e32 v54, -1, v50
	v_add_u32_e32 v55, 1, v50
	v_add_u32_e32 v56, -1, v51
	v_add_u32_e32 v58, -1, v52
	v_fma_f32 v62, -v54, v50, v46
	v_add_u32_e32 v57, 1, v51
	v_add_u32_e32 v59, 1, v52
	v_fma_f32 v63, -v55, v50, v46
	v_fma_f32 v64, -v56, v51, v47
	v_fma_f32 v66, -v58, v52, v48
	v_cmp_ge_f32_e64 s[8:9], 0, v62
	v_add_u32_e32 v60, -1, v53
	v_fma_f32 v65, -v57, v51, v47
	v_fma_f32 v67, -v59, v52, v48
	v_cndmask_b32_e64 v50, v50, v54, s[8:9]
	v_cmp_ge_f32_e64 s[8:9], 0, v64
	v_cmp_ge_f32_e64 s[10:11], 0, v66
	v_cmp_lt_f32_e64 s[14:15], 0, v63
	v_add_u32_e32 v61, 1, v53
	v_fma_f32 v68, -v60, v53, v49
	v_cndmask_b32_e64 v51, v51, v56, s[8:9]
	v_cmp_lt_f32_e64 s[8:9], 0, v65
	v_cndmask_b32_e64 v52, v52, v58, s[10:11]
	v_cmp_lt_f32_e64 s[10:11], 0, v67
	v_cndmask_b32_e64 v50, v50, v55, s[14:15]
	v_fma_f32 v69, -v61, v53, v49
	v_cmp_ge_f32_e64 s[12:13], 0, v68
	v_cndmask_b32_e64 v51, v51, v57, s[8:9]
	v_cndmask_b32_e64 v52, v52, v59, s[10:11]
	v_mul_f32_e32 v54, 0x37800000, v50
	v_cndmask_b32_e64 v53, v53, v60, s[12:13]
	v_cmp_lt_f32_e64 s[12:13], 0, v69
	v_mul_f32_e32 v55, 0x37800000, v51
	v_mul_f32_e32 v56, 0x37800000, v52
	v_cndmask_b32_e64 v50, v50, v54, s[6:7]
	v_cmp_class_f32_e64 s[6:7], v46, v29
	v_cndmask_b32_e64 v53, v53, v61, s[12:13]
	v_cndmask_b32_e32 v51, v51, v55, vcc
	v_cmp_class_f32_e32 vcc, v47, v29
	v_cndmask_b32_e64 v52, v52, v56, s[0:1]
	v_cmp_class_f32_e64 s[0:1], v48, v29
	v_cndmask_b32_e64 v46, v50, v46, s[6:7]
	v_mul_f32_e32 v57, 0x37800000, v53
	v_cndmask_b32_e32 v47, v51, v47, vcc
	v_cndmask_b32_e64 v48, v52, v48, s[0:1]
	v_div_scale_f32 v50, s[0:1], v46, v46, 1.0
	v_cndmask_b32_e64 v53, v53, v57, s[4:5]
	v_div_scale_f32 v52, s[0:1], v47, v47, 1.0
	v_rcp_f32_e32 v57, v50
	v_rcp_f32_e32 v58, v52
	v_cmp_class_f32_e64 s[4:5], v49, v29
	v_div_scale_f32 v51, vcc, 1.0, v46, 1.0
	v_fma_f32 v59, -v50, v57, 1.0
	v_fma_f32 v60, -v52, v58, 1.0
	v_fmac_f32_e32 v57, v59, v57
	v_cndmask_b32_e64 v49, v53, v49, s[4:5]
	v_div_scale_f32 v53, s[4:5], 1.0, v47, 1.0
	v_fmac_f32_e32 v58, v60, v58
	v_mul_f32_e32 v59, v51, v57
	v_mul_f32_e32 v60, v53, v58
	v_fma_f32 v61, -v50, v59, v51
	v_fma_f32 v62, -v52, v60, v53
	v_fmac_f32_e32 v59, v61, v57
	v_fmac_f32_e32 v60, v62, v58
	v_fma_f32 v50, -v50, v59, v51
	v_fma_f32 v51, -v52, v60, v53
	v_div_fmas_f32 v50, v50, v57, v59
	s_mov_b64 vcc, s[4:5]
	v_div_fixup_f32 v46, v50, v46, 1.0
	v_div_fmas_f32 v50, v51, v58, v60
	v_div_fixup_f32 v47, v50, v47, 1.0
	s_nop 0
	v_mul_f32_e32 v50, v46, v6
	v_mul_f32_e32 v6, v6, v47
	v_mul_f32_e32 v51, v46, v7
	v_mul_f32_e32 v7, v7, v47
	v_mul_f32_e32 v52, v46, v8
	v_mul_f32_e32 v8, v8, v47
	v_mul_f32_e32 v53, v46, v9
	v_mul_f32_e32 v9, v9, v47
	v_mul_f32_e32 v57, v46, v2
	v_mul_f32_e32 v2, v47, v2
	v_mul_f32_e32 v58, v46, v3
	v_mul_f32_e32 v3, v47, v3
	v_mul_f32_e32 v59, v46, v4
	v_mul_f32_e32 v4, v47, v4
	v_mul_f32_e32 v46, v46, v5
	v_mul_f32_e32 v5, v47, v5
	s_nop 0
	v_lshlrev_b32_e32 v47, 16, v34
	v_and_b32_e32 v34, 0xffff0000, v34
	v_lshlrev_b32_e32 v60, 16, v35
	v_and_b32_e32 v35, 0xffff0000, v35
	v_lshlrev_b32_e32 v61, 16, v36
	v_and_b32_e32 v36, 0xffff0000, v36
	v_lshlrev_b32_e32 v62, 16, v37
	v_and_b32_e32 v37, 0xffff0000, v37
	s_nop 0
	v_lshlrev_b32_e32 v63, 16, v38
	v_and_b32_e32 v38, 0xffff0000, v38
	v_lshlrev_b32_e32 v64, 16, v39
	v_and_b32_e32 v39, 0xffff0000, v39
	v_lshlrev_b32_e32 v65, 16, v40
	v_and_b32_e32 v40, 0xffff0000, v40
	v_lshlrev_b32_e32 v66, 16, v41
	v_and_b32_e32 v41, 0xffff0000, v41
	v_mul_f32_e32 v47, v50, v47
	v_mul_f32_e32 v34, v51, v34
	v_mul_f32_e32 v7, v7, v38
	v_mul_f32_e32 v38, v52, v60
	v_mul_f32_e32 v35, v53, v35
	v_mul_f32_e32 v9, v9, v39
	v_mul_f32_e32 v39, v57, v61
	v_mul_f32_e32 v50, v2, v65
	v_mul_f32_e32 v36, v58, v36
	v_mul_f32_e32 v40, v3, v40
	v_mul_f32_e32 v51, v59, v62
	v_mul_f32_e32 v52, v4, v66
	v_mul_f32_e32 v37, v46, v37
	v_mul_f32_e32 v41, v5, v41
	v_cvt_pk_bf16_f32 v2, v47, v34
	v_cvt_pk_bf16_f32 v3, v38, v35
	v_cvt_pk_bf16_f32 v4, v39, v36
	v_cvt_pk_bf16_f32 v5, v51, v37
	v_mul_f32_e32 v6, v6, v63
	v_mul_f32_e32 v8, v8, v64
	global_store_dwordx4 v[42:43], v[2:5], off
	v_div_scale_f32 v54, s[0:1], v48, v48, 1.0
	s_nop 0
	v_cvt_pk_bf16_f32 v2, v6, v7
	v_cvt_pk_bf16_f32 v3, v8, v9
	v_cvt_pk_bf16_f32 v4, v50, v40
	v_cvt_pk_bf16_f32 v5, v52, v41
	global_store_dwordx4 v[44:45], v[2:5], off
	s_waitcnt vmcnt(8)
; #define GAS __attribute__((address_space(1)))
; __device__ __forceinline__ unsigned xb_ld(unsigned* p)              { return __hip_atomic_load(p, __ATOMIC_RELAXED, __HIP_MEMORY_SCOPE_AGENT); }
; __device__ __forceinline__ void xcd_barrier_complete(unsigned* bar, unsigned x, unsigned& nloc, unsigned& nx) {
;     const unsigned G = gridDim.x * gridDim.y * gridDim.z;
;     unsigned sum, cnt, mine, sp = 0u;
;     for (;;) {
;         sum = 0u; cnt = 0u; mine = 0u;
; #pragma unroll
;         for (unsigned j = 0; j < 16; ++j) { const unsigned c = xb_ld(&bar[XB_XCNT(j)]); sum += c; cnt += (c > 0u) ? 1u : 0u; mine = (j == x) ? c : mine; }
;         if (sum == G) break;
;         __builtin_amdgcn_s_sleep(1);
;         if ((++sp & 255u) == 0u) { if (xb_ld(&bar[XB_TMO])) break; if (sp > XB_SPIN_CAP) { atomicAdd(&bar[XB_TMO], 1u); break; } }
;     }
;     nloc = mine > 0u ? mine : 1u; nx = cnt > 0u ? cnt : 1u;
; }
; __device__ __forceinline__ void xcd_barrier(const XcdBarrier& b) {
;     asm volatile("s_waitcnt vmcnt(0)" ::: "memory");
;     __syncthreads();
;     if (threadIdx.x == 0) {
;         unsigned* bar = b.bar;
;         __builtin_amdgcn_s_waitcnt(0);
;         unsigned nloc = b.st[0], nx = b.st[1];
;         if (nloc == 0u) { xcd_barrier_complete(bar, b.x, nloc, nx); b.st[0] = nloc; b.st[1] = nx; }
; __device__ __forceinline__ void p3_rows2(int row0, const bf16* PROJ, const float* sc_w, const float* sc_nw, const float* ssd_nw, const float* SSQ, bf16* Y, LAS unsigned char* scr, int lane) {
;     ...
; #pragma unroll 2
;     for (int i = 0; i < 8; ++i) { const int c0 = (i * 64 + lane) * 8;
;         const float rg0 = 1.0f / sqrtf(__shfl(gs0, i * 8) * (1.f / 512.f) + EPS), rg1 = 1.0f / sqrtf(__shfl(gs1, i * 8) * (1.f / 512.f) + EPS);
;         float f0[8], f1[8]; unpack8(*(const GAS u32x4*)(yrow + i * 512), f0); unpack8(*(const GAS u32x4*)(yrow + D_MIX + i * 512), f1);
;         const f32x4 ga = *(const GAS f32x4*)(ssd_nw + c0), gb = *(const GAS f32x4*)(ssd_nw + c0 + 4); const float g[8] = {ga.x, ga.y, ga.z, ga.w, gb.x, gb.y, gb.z, gb.w};
; #pragma unroll
;         for (int j = 0; j < 8; ++j) { f0[j] *= rg0 * g[j]; f1[j] *= rg1 * g[j]; }
;         *(GAS u32x4*)(yrow + i * 512) = pack8(f0); *(GAS u32x4*)(yrow + D_MIX + i * 512) = pack8(f1); }
	v_mov_b32_e32 v6, v200
	v_mov_b32_e32 v7, v201
	v_mov_b32_e32 v8, v202
	v_mov_b32_e32 v9, v203
	s_nop 0
	v_mov_b32_e32 v2, v204
	v_mov_b32_e32 v3, v205
	v_mov_b32_e32 v4, v206
	v_mov_b32_e32 v5, v207
	v_mov_b32_e32 v34, v208
	v_mov_b32_e32 v35, v209
	v_mov_b32_e32 v36, v210
	v_mov_b32_e32 v37, v211
	v_mov_b32_e32 v38, v212
	v_mov_b32_e32 v39, v213
	v_mov_b32_e32 v40, v214
	v_mov_b32_e32 v41, v215
	global_load_dwordx4 v[200:203], v[216:217], off offset:1024
	global_load_dwordx4 v[204:207], v[220:221], off
	global_load_dwordx4 v[208:211], v[220:221], off offset:-16
	global_load_dwordx4 v[212:215], v[218:219], off offset:1024
	v_div_scale_f32 v56, s[6:7], v49, v49, 1.0
	v_rcp_f32_e32 v47, v54
	v_rcp_f32_e32 v50, v56
	v_div_scale_f32 v55, s[0:1], 1.0, v48, 1.0
	v_fma_f32 v51, -v54, v47, 1.0
	v_fma_f32 v52, -v56, v50, 1.0
	v_fmac_f32_e32 v47, v51, v47
	v_div_scale_f32 v46, s[4:5], 1.0, v49, 1.0
	v_fmac_f32_e32 v50, v52, v50
	v_mul_f32_e32 v51, v55, v47
	v_mul_f32_e32 v52, v46, v50
	v_fma_f32 v53, -v54, v51, v55
	v_fma_f32 v57, -v56, v52, v46
	v_fmac_f32_e32 v51, v53, v47
	v_fmac_f32_e32 v52, v57, v50
	v_fma_f32 v53, -v54, v51, v55
	s_mov_b64 vcc, s[0:1]
	v_fma_f32 v46, -v56, v52, v46
	v_div_fmas_f32 v47, v53, v47, v51
	s_mov_b64 vcc, s[4:5]
	v_div_fmas_f32 v46, v46, v50, v52
	s_add_u32 s30, s30, 0x800
	v_div_fixup_f32 v47, v47, v48, 1.0
	v_div_fixup_f32 v46, v46, v49, 1.0
	s_addc_u32 s31, s31, 0
	v_add_u32_e32 v31, 64, v31
	s_cmpk_lg_i32 s30, 0x2000
	v_lshl_add_u64 v[26:27], v[26:27], 0, s[26:27]
	s_nop 0
	v_mul_f32_e32 v60, v47, v2
	v_lshlrev_b32_e32 v48, 16, v6
	v_and_b32_e32 v6, 0xffff0000, v6
	v_lshlrev_b32_e32 v49, 16, v7
	v_and_b32_e32 v7, 0xffff0000, v7
	v_lshlrev_b32_e32 v50, 16, v8
	v_and_b32_e32 v8, 0xffff0000, v8
	v_lshlrev_b32_e32 v51, 16, v9
	v_and_b32_e32 v9, 0xffff0000, v9
	s_nop 0
	v_lshlrev_b32_e32 v52, 16, v38
	v_and_b32_e32 v38, 0xffff0000, v38
	v_lshlrev_b32_e32 v53, 16, v39
	v_and_b32_e32 v39, 0xffff0000, v39
	v_lshlrev_b32_e32 v54, 16, v40
	v_and_b32_e32 v40, 0xffff0000, v40
	v_lshlrev_b32_e32 v55, 16, v41
	v_and_b32_e32 v41, 0xffff0000, v41
	v_mul_f32_e32 v56, v47, v34
	v_mul_f32_e32 v57, v47, v35
	v_mul_f32_e32 v35, v35, v46
	v_mul_f32_e32 v58, v47, v36
	v_mul_f32_e32 v59, v47, v37
	v_mul_f32_e32 v37, v37, v46
	v_mul_f32_e32 v2, v46, v2
	v_mul_f32_e32 v61, v47, v3
	v_mul_f32_e32 v3, v46, v3
	v_mul_f32_e32 v62, v47, v4
	v_mul_f32_e32 v4, v46, v4
	v_mul_f32_e32 v47, v47, v5
	v_mul_f32_e32 v5, v46, v5
	v_mul_f32_e32 v34, v34, v46
	v_mul_f32_e32 v36, v36, v46
	v_mul_f32_e32 v46, v56, v48
	v_mul_f32_e32 v6, v57, v6
	v_mul_f32_e32 v35, v35, v38
	v_mul_f32_e32 v38, v58, v49
	v_mul_f32_e32 v7, v59, v7
	v_mul_f32_e32 v37, v37, v39
	v_mul_f32_e32 v39, v60, v50
	v_mul_f32_e32 v48, v2, v54
	v_mul_f32_e32 v8, v61, v8
	v_mul_f32_e32 v40, v3, v40
	v_mul_f32_e32 v49, v62, v51
	v_mul_f32_e32 v50, v4, v55
	v_mul_f32_e32 v9, v47, v9
	v_mul_f32_e32 v41, v5, v41
	v_cvt_pk_bf16_f32 v2, v46, v6
	v_cvt_pk_bf16_f32 v3, v38, v7
	v_cvt_pk_bf16_f32 v4, v39, v8
	v_cvt_pk_bf16_f32 v5, v49, v9
	v_mul_f32_e32 v34, v34, v52
	v_mul_f32_e32 v36, v36, v53
	global_store_dwordx4 v[42:43], v[2:5], off offset:1024
	s_nop 1
	v_cvt_pk_bf16_f32 v2, v34, v35
	v_cvt_pk_bf16_f32 v3, v36, v37
	v_cvt_pk_bf16_f32 v4, v48, v40
	v_cvt_pk_bf16_f32 v5, v50, v41
	global_store_dwordx4 v[44:45], v[2:5], off offset:1024
	s_cbranch_scc1 .LBB0_489
	s_add_i32 s41, s41, s46
	s_add_i32 s16, s16, s33
	s_cmpk_gt_i32 s41, 0x1fff
	s_cbranch_scc0 .LBB0_484
.LBB0_491:
	s_waitcnt vmcnt(0)
	v_readlane_b32 s12, v249, 2
	v_readlane_b32 s13, v249, 3
	s_cmp_gt_i32 s13, 4
	s_cbranch_scc0 .LBB0_545
	s_waitcnt vmcnt(0)
	s_waitcnt vmcnt(0)
	s_barrier
	s_mov_b64 s[0:1], exec
	v_readlane_b32 s2, v249, 7
	v_readlane_b32 s3, v249, 8
	s_and_b64 s[2:3], s[0:1], s[2:3]
	s_mov_b64 exec, s[2:3]
	s_cbranch_execz .LBB0_544
	s_add_i32 s2, 0, 0x20160
	v_mov_b32_e32 v1, s2
	s_waitcnt vmcnt(0) expcnt(0) lgkmcnt(0)
	ds_read_b32 v3, v1
	s_add_i32 s2, 0, 0x20164
	v_mov_b32_e32 v1, s2
	ds_read_b32 v1, v1
	s_waitcnt lgkmcnt(1)
	v_cmp_ne_u32_e32 vcc, 0, v3
	s_cbranch_vccnz .LBB0_508
	v_readlane_b32 s2, v249, 0
	v_readlane_b32 s3, v249, 1
	s_load_dwordx2 s[6:7], s[2:3], 0x4
	s_add_u32 s2, s70, 0x4200
	s_addc_u32 s3, s71, 0
	s_add_u32 s4, s70, 0x4400
	s_addc_u32 s5, s71, 0
	s_waitcnt lgkmcnt(0)
	s_mul_i32 s33, s6, s78
	s_add_u32 s6, s70, 0x4500
	s_mul_i32 s33, s33, s7
	s_addc_u32 s7, s71, 0
	s_add_u32 s8, s70, 0x4600
	s_addc_u32 s9, s71, 0
	s_add_u32 s10, s70, 0x4700
	s_addc_u32 s11, s71, 0
	s_add_u32 s12, s70, 0x4800
	s_addc_u32 s13, s71, 0
	s_add_u32 s14, s70, 0x4900
	s_addc_u32 s15, s71, 0
	s_add_u32 s16, s70, 0x4a00
	s_addc_u32 s17, s71, 0
	s_add_u32 s18, s70, 0x4b00
	s_addc_u32 s19, s71, 0
	s_add_u32 s20, s70, 0x4c00
	s_addc_u32 s21, s71, 0
	s_add_u32 s22, s70, 0x4d00
	s_addc_u32 s23, s71, 0
	s_add_u32 s24, s70, 0x4e00
	s_addc_u32 s25, s71, 0
	s_add_u32 s26, s70, 0x4f00
	s_addc_u32 s27, s71, 0
	s_add_u32 s28, s70, 0x5000
	s_addc_u32 s29, s71, 0
	s_add_u32 s30, s70, 0x5100
	s_addc_u32 s31, s71, 0
	s_add_u32 s34, s70, 0x5200
	s_addc_u32 s35, s71, 0
	s_add_u32 s36, s70, 0x5300
	s_addc_u32 s37, s71, 0
	s_mov_b32 s44, 1
	v_mov_b32_e32 v17, 0
	s_branch .LBB0_496
